# MoE fused GEMM: first K trip uses literal-0 accumulator input in its two first-touch MFMA segments; per-unit accumulator clear removed (on top of v100)
# baseline (speedup 1.0000x reference)
.LBB0_1412:
	s_add_u32 s8, s18, 0x1fc00000
	s_addc_u32 s6, s19, 0
	s_add_u32 s12, s18, 0x1b400000
	v_and_b32_e32 v1, 15, v196
	v_and_b32_e32 v2, 48, v196
	s_addc_u32 s7, s19, 0
	s_lshl_b32 s9, s4, 6
	v_lshl_or_b32 v1, v1, 6, v2
	v_lshlrev_b32_e32 v2, 2, v196
	s_and_b32 s5, s5, 3
	v_writelane_b32 v253, s9, 61
	s_lshl_b32 s9, s4, 13
	v_and_b32_e32 v2, 32, v2
	v_bitop3_b32 v3, v1, s9, v2 bitop3:0xde
	s_lshl_b32 s9, s5, 5
	v_writelane_b32 v253, s9, 63
	s_lshl_b32 s9, s5, 12
	s_add_i32 s83, s73, 0x18000
	v_bitop3_b32 v1, s9, v1, v2 bitop3:0xf6
	s_add_i32 s9, s66, 0x80
	s_mov_b32 m0, s83
	s_add_i32 s84, s73, 0x1a000
	s_waitcnt vmcnt(2)
	s_barrier
	buffer_load_dwordx4 v194, s[60:63], s9 offen lds
	s_add_i32 s9, s9, s2
	s_mov_b32 m0, s84
	s_add_i32 s85, s73, 0x8000
	buffer_load_dwordx4 v194, s[60:63], s9 offen lds
	s_add_i32 s9, s57, 0x80
	s_mov_b32 m0, s85
	s_add_i32 s86, s73, 0xa000
	buffer_load_dwordx4 v192, s[60:63], s9 offen lds
	s_add_i32 s9, s9, s2
	s_mov_b32 m0, s86
	s_add_i32 s87, s73, 0x1c000
	buffer_load_dwordx4 v192, s[60:63], s9 offen lds
	s_addk_i32 s3, 0x80
	s_mov_b32 m0, s87
	s_add_i32 s90, s73, 0x1e000
	buffer_load_dwordx4 v194, s[60:63], s3 offen lds
	s_add_i32 s3, s3, s2
	s_mov_b32 m0, s90
	s_cmp_lt_u32 s10, 64
	buffer_load_dwordx4 v194, s[60:63], s3 offen lds
	s_cselect_b64 s[24:25], -1, 0
	s_add_i32 s91, s73, 0xc000
	s_add_i32 s92, s73, 0xe000
	s_cmpk_lt_u32 s10, 0x100
	s_cselect_b64 s[26:27], -1, 0
	s_and_b32 s13, s7, 0xffff
	s_lshl_b32 s5, s5, 6
	s_lshl_b32 s94, s4, 17
	s_and_b32 s9, s6, 0xffff
	s_cmp_lt_i32 s95, s1
	v_writelane_b32 v253, s5, 56
	s_cselect_b64 s[4:5], -1, 0
	v_cmp_eq_u32_e64 s[2:3], 0, v0
	v_cndmask_b32_e64 v0, 0, 1, s[4:5]
	s_cmp_lt_i32 s95, s0
	v_readfirstlane_b32 s4, v0
	s_waitcnt vmcnt(6)
	v_or_b32_e32 v1, 0x10000, v1
	s_mov_b32 s10, -1
	v_writelane_b32 v254, s4, 5
	s_cselect_b32 s4, 0, 3
	s_sub_i32 s5, s93, s0
	s_sub_i32 s0, s95, s0
	v_writelane_b32 v254, s4, 7
	s_mul_i32 s4, s51, s93
	s_add_i32 s0, s0, s1
	v_writelane_b32 v254, s5, 11
	s_add_i32 s0, s0, s4
	v_writelane_b32 v254, s0, 13
	s_add_i32 s0, s4, s95
	s_mov_b32 s36, 0
	s_mov_b32 s11, s63
	v_writelane_b32 v254, s0, 9
	v_add_u32_e32 v199, 0, v1
	v_add_u32_e32 v200, 0, v3
	s_mov_b32 s64, s10
	s_barrier
	s_branch .LBB0_1415
.LBB0_1413:
	s_mov_b32 s52, s37
	s_mov_b32 s53, s1
	s_mov_b32 s97, s54
	s_mov_b32 s55, s48
	s_mov_b32 s66, s67
	s_mov_b32 s57, s56
	s_mov_b32 s72, s46
	s_mov_b32 s36, s95
.LBB0_1414:
	s_andn2_b64 vcc, exec, s[28:29]
	s_cbranch_vccz .LBB0_1485

.LBB0_1441:
	s_addk_i32 s42, 0x100
	s_add_i32 s43, s42, s66
	s_and_b64 s[40:41], s[38:39], exec
	s_waitcnt vmcnt(8)
	s_cselect_b32 s41, s67, s43
	s_add_i32 s42, s42, s57
	s_waitcnt lgkmcnt(0)
	s_and_b64 s[38:39], s[38:39], exec
	s_cselect_b32 s40, s56, s42
	s_add_i32 s38, s41, 0x80
	s_add_i32 s39, s40, 0x80
	s_barrier
	s_cmp_eq_u32 s82, 0
	s_cbranch_scc1 .Lc0_moe_1
	s_setprio 1
	s_waitcnt lgkmcnt(6)
	v_mfma_scale_f32_16x16x128_f8f6f4 v[188:191], v[16:23], v[56:63], v[188:191], v238, v238 op_sel_hi:[0,0,0]
	v_mfma_scale_f32_16x16x128_f8f6f4 v[184:187], v[24:31], v[56:63], v[184:187], v238, v238 op_sel_hi:[0,0,0]
	s_waitcnt lgkmcnt(4)
	v_mfma_scale_f32_16x16x128_f8f6f4 v[180:183], v[16:23], v[48:55], v[180:183], v238, v238 op_sel_hi:[0,0,0]
	v_mfma_scale_f32_16x16x128_f8f6f4 v[176:179], v[24:31], v[48:55], v[176:179], v238, v238 op_sel_hi:[0,0,0]
	s_waitcnt lgkmcnt(2)
	v_mfma_scale_f32_16x16x128_f8f6f4 v[172:175], v[16:23], v[40:47], v[172:175], v238, v238 op_sel_hi:[0,0,0]
	v_mfma_scale_f32_16x16x128_f8f6f4 v[168:171], v[24:31], v[40:47], v[168:171], v238, v238 op_sel_hi:[0,0,0]
	s_waitcnt lgkmcnt(0)
	v_mfma_scale_f32_16x16x128_f8f6f4 v[164:167], v[16:23], v[32:39], v[164:167], v238, v238 op_sel_hi:[0,0,0]
	v_mfma_scale_f32_16x16x128_f8f6f4 v[160:163], v[24:31], v[32:39], v[160:163], v238, v238 op_sel_hi:[0,0,0]
	s_setprio 0
	s_setprio 1
	v_mfma_scale_f32_16x16x128_f8f6f4 v[156:159], v[0:7], v[56:63], v[156:159], v238, v238 op_sel_hi:[0,0,0]
	v_mfma_scale_f32_16x16x128_f8f6f4 v[152:155], v[8:15], v[56:63], v[152:155], v238, v238 op_sel_hi:[0,0,0]
	v_mfma_scale_f32_16x16x128_f8f6f4 v[148:151], v[0:7], v[48:55], v[148:151], v238, v238 op_sel_hi:[0,0,0]
	v_mfma_scale_f32_16x16x128_f8f6f4 v[144:147], v[8:15], v[48:55], v[144:147], v238, v238 op_sel_hi:[0,0,0]
	v_mfma_scale_f32_16x16x128_f8f6f4 v[140:143], v[0:7], v[40:47], v[140:143], v238, v238 op_sel_hi:[0,0,0]
	v_mfma_scale_f32_16x16x128_f8f6f4 v[136:139], v[8:15], v[40:47], v[136:139], v238, v238 op_sel_hi:[0,0,0]
	v_mfma_scale_f32_16x16x128_f8f6f4 v[132:135], v[0:7], v[32:39], v[132:135], v238, v238 op_sel_hi:[0,0,0]
	v_mfma_scale_f32_16x16x128_f8f6f4 v[128:131], v[8:15], v[32:39], v[128:131], v238, v238 op_sel_hi:[0,0,0]
	s_setprio 0
.Lc0_moe_1_join:
	s_barrier
	s_mov_b32 m0, s74
	s_lshl_b32 s42, s50, 6
	ds_read_b128 v[32:35], v200 offset:16384
	ds_read_b128 v[36:39], v200 offset:17408
	ds_read_b128 v[40:43], v200 offset:18432
	ds_read_b128 v[44:47], v200 offset:19456
	ds_read_b128 v[48:51], v200 offset:20480
	ds_read_b128 v[52:55], v200 offset:21504
	ds_read_b128 v[56:59], v200 offset:22528
	ds_read_b128 v[60:63], v200 offset:23552
	buffer_load_dwordx4 v194, s[60:63], s41 offen lds
	s_add_i32 s41, s42, s41
	s_mov_b32 m0, s75
	s_nop 0
	buffer_load_dwordx4 v194, s[60:63], s41 offen lds
	s_add_i32 s41, s41, s42
	s_mov_b32 m0, s76
	s_nop 0
	buffer_load_dwordx4 v194, s[60:63], s41 offen lds
	s_add_i32 s41, s41, s42
	s_mov_b32 m0, s77
	s_nop 0
	buffer_load_dwordx4 v194, s[60:63], s41 offen lds
	s_mov_b32 m0, s73
	s_nop 0
	buffer_load_dwordx4 v192, s[60:63], s40 offen lds
	s_add_i32 s40, s42, s40
	s_mov_b32 m0, s78
	s_nop 0
	buffer_load_dwordx4 v192, s[60:63], s40 offen lds
	s_waitcnt vmcnt(8)
	s_waitcnt lgkmcnt(0)
	s_barrier
	s_cmp_eq_u32 s82, 0
	s_cbranch_scc1 .Lc0_moe_2
	s_setprio 1
	s_waitcnt lgkmcnt(6)
	v_mfma_scale_f32_16x16x128_f8f6f4 v[124:127], v[16:23], v[32:39], v[124:127], v238, v238 op_sel_hi:[0,0,0]
	v_mfma_scale_f32_16x16x128_f8f6f4 v[120:123], v[24:31], v[32:39], v[120:123], v238, v238 op_sel_hi:[0,0,0]
	s_waitcnt lgkmcnt(4)
	v_mfma_scale_f32_16x16x128_f8f6f4 v[116:119], v[16:23], v[40:47], v[116:119], v238, v238 op_sel_hi:[0,0,0]
	v_mfma_scale_f32_16x16x128_f8f6f4 v[112:115], v[24:31], v[40:47], v[112:115], v238, v238 op_sel_hi:[0,0,0]
	s_waitcnt lgkmcnt(2)
	v_mfma_scale_f32_16x16x128_f8f6f4 v[108:111], v[16:23], v[48:55], v[108:111], v238, v238 op_sel_hi:[0,0,0]
	v_mfma_scale_f32_16x16x128_f8f6f4 v[104:107], v[24:31], v[48:55], v[104:107], v238, v238 op_sel_hi:[0,0,0]
	s_waitcnt lgkmcnt(0)
	v_mfma_scale_f32_16x16x128_f8f6f4 v[100:103], v[16:23], v[56:63], v[100:103], v238, v238 op_sel_hi:[0,0,0]
	v_mfma_scale_f32_16x16x128_f8f6f4 v[96:99], v[24:31], v[56:63], v[96:99], v238, v238 op_sel_hi:[0,0,0]
	s_setprio 0
	s_setprio 1
	v_mfma_scale_f32_16x16x128_f8f6f4 v[92:95], v[0:7], v[32:39], v[92:95], v238, v238 op_sel_hi:[0,0,0]
	v_mfma_scale_f32_16x16x128_f8f6f4 v[88:91], v[8:15], v[32:39], v[88:91], v238, v238 op_sel_hi:[0,0,0]
	v_mfma_scale_f32_16x16x128_f8f6f4 v[84:87], v[0:7], v[40:47], v[84:87], v238, v238 op_sel_hi:[0,0,0]
	v_mfma_scale_f32_16x16x128_f8f6f4 v[80:83], v[8:15], v[40:47], v[80:83], v238, v238 op_sel_hi:[0,0,0]
	v_mfma_scale_f32_16x16x128_f8f6f4 v[76:79], v[0:7], v[48:55], v[76:79], v238, v238 op_sel_hi:[0,0,0]
	v_mfma_scale_f32_16x16x128_f8f6f4 v[72:75], v[8:15], v[48:55], v[72:75], v238, v238 op_sel_hi:[0,0,0]
	v_mfma_scale_f32_16x16x128_f8f6f4 v[68:71], v[0:7], v[56:63], v[68:71], v238, v238 op_sel_hi:[0,0,0]
	v_mfma_scale_f32_16x16x128_f8f6f4 v[64:67], v[8:15], v[56:63], v[64:67], v238, v238 op_sel_hi:[0,0,0]
	s_setprio 0
.Lc0_moe_2_join:
	s_barrier
	ds_read_b128 v[0:3], v199 offset:32768
	ds_read_b128 v[4:7], v199 offset:33792
	ds_read_b128 v[8:11], v199 offset:34816
	ds_read_b128 v[12:15], v199 offset:35840
	ds_read_b128 v[16:19], v199 offset:49152
	ds_read_b128 v[20:23], v199 offset:50176
	ds_read_b128 v[24:27], v199 offset:51200
	ds_read_b128 v[28:31], v199 offset:52224
	s_mov_b32 m0, s79
	s_add_i32 s40, s40, s42
	ds_read_b128 v[32:35], v200 offset:32768
	ds_read_b128 v[36:39], v200 offset:33792
	ds_read_b128 v[40:43], v200 offset:34816
	ds_read_b128 v[44:47], v200 offset:35840
	ds_read_b128 v[48:51], v200 offset:36864
	ds_read_b128 v[52:55], v200 offset:37888
	ds_read_b128 v[56:59], v200 offset:38912
	ds_read_b128 v[60:63], v200 offset:39936
	buffer_load_dwordx4 v192, s[60:63], s40 offen lds
	s_add_i32 s40, s40, s42
	s_mov_b32 m0, s80
	s_nop 0
	buffer_load_dwordx4 v192, s[60:63], s40 offen lds
	s_waitcnt vmcnt(8)
	s_waitcnt lgkmcnt(0)
	s_barrier
	s_setprio 1
	s_waitcnt lgkmcnt(6)
	v_mfma_scale_f32_16x16x128_f8f6f4 v[188:191], v[0:7], v[32:39], v[188:191], v238, v238 op_sel_hi:[0,0,0]
	v_mfma_scale_f32_16x16x128_f8f6f4 v[184:187], v[8:15], v[32:39], v[184:187], v238, v238 op_sel_hi:[0,0,0]
	s_waitcnt lgkmcnt(4)
	v_mfma_scale_f32_16x16x128_f8f6f4 v[180:183], v[0:7], v[40:47], v[180:183], v238, v238 op_sel_hi:[0,0,0]
	v_mfma_scale_f32_16x16x128_f8f6f4 v[176:179], v[8:15], v[40:47], v[176:179], v238, v238 op_sel_hi:[0,0,0]
	s_waitcnt lgkmcnt(2)
	v_mfma_scale_f32_16x16x128_f8f6f4 v[172:175], v[0:7], v[48:55], v[172:175], v238, v238 op_sel_hi:[0,0,0]
	v_mfma_scale_f32_16x16x128_f8f6f4 v[168:171], v[8:15], v[48:55], v[168:171], v238, v238 op_sel_hi:[0,0,0]
	s_waitcnt lgkmcnt(0)
	v_mfma_scale_f32_16x16x128_f8f6f4 v[164:167], v[0:7], v[56:63], v[164:167], v238, v238 op_sel_hi:[0,0,0]
	v_mfma_scale_f32_16x16x128_f8f6f4 v[160:163], v[8:15], v[56:63], v[160:163], v238, v238 op_sel_hi:[0,0,0]
	s_setprio 0
	s_setprio 1
	v_mfma_scale_f32_16x16x128_f8f6f4 v[156:159], v[16:23], v[32:39], v[156:159], v238, v238 op_sel_hi:[0,0,0]
	v_mfma_scale_f32_16x16x128_f8f6f4 v[152:155], v[24:31], v[32:39], v[152:155], v238, v238 op_sel_hi:[0,0,0]
	v_mfma_scale_f32_16x16x128_f8f6f4 v[148:151], v[16:23], v[40:47], v[148:151], v238, v238 op_sel_hi:[0,0,0]
	v_mfma_scale_f32_16x16x128_f8f6f4 v[144:147], v[24:31], v[40:47], v[144:147], v238, v238 op_sel_hi:[0,0,0]
	v_mfma_scale_f32_16x16x128_f8f6f4 v[140:143], v[16:23], v[48:55], v[140:143], v238, v238 op_sel_hi:[0,0,0]
	v_mfma_scale_f32_16x16x128_f8f6f4 v[136:139], v[24:31], v[48:55], v[136:139], v238, v238 op_sel_hi:[0,0,0]
	v_mfma_scale_f32_16x16x128_f8f6f4 v[132:135], v[16:23], v[56:63], v[132:135], v238, v238 op_sel_hi:[0,0,0]
	v_mfma_scale_f32_16x16x128_f8f6f4 v[128:131], v[24:31], v[56:63], v[128:131], v238, v238 op_sel_hi:[0,0,0]
	s_setprio 0
	s_barrier
	s_mov_b32 m0, s83
	ds_read_b128 v[32:35], v200 offset:49152
	ds_read_b128 v[36:39], v200 offset:50176
	ds_read_b128 v[40:43], v200 offset:51200
	ds_read_b128 v[44:47], v200 offset:52224
	ds_read_b128 v[48:51], v200 offset:53248
	ds_read_b128 v[52:55], v200 offset:54272
	ds_read_b128 v[56:59], v200 offset:55296
	ds_read_b128 v[60:63], v200 offset:56320
	buffer_load_dwordx4 v194, s[60:63], s38 offen lds
	s_add_i32 s38, s42, s38
	s_mov_b32 m0, s84
	s_nop 0
	buffer_load_dwordx4 v194, s[60:63], s38 offen lds
	s_add_i32 s38, s38, s42
	s_mov_b32 m0, s87
	s_nop 0
	buffer_load_dwordx4 v194, s[60:63], s38 offen lds
	s_add_i32 s38, s38, s42
	s_mov_b32 m0, s90
	s_add_i32 s42, s42, s39
	buffer_load_dwordx4 v194, s[60:63], s38 offen lds
	s_mov_b32 m0, s85
	s_nop 0
	buffer_load_dwordx4 v192, s[60:63], s39 offen lds
	s_mov_b32 m0, s86
	s_nop 0
	buffer_load_dwordx4 v192, s[60:63], s42 offen lds
	s_waitcnt vmcnt(8)
	s_waitcnt lgkmcnt(0)
	s_barrier
	s_setprio 1
	s_waitcnt lgkmcnt(6)
	v_mfma_scale_f32_16x16x128_f8f6f4 v[124:127], v[0:7], v[32:39], v[124:127], v238, v238 op_sel_hi:[0,0,0]
	v_mfma_scale_f32_16x16x128_f8f6f4 v[120:123], v[8:15], v[32:39], v[120:123], v238, v238 op_sel_hi:[0,0,0]
	s_waitcnt lgkmcnt(4)
	v_mfma_scale_f32_16x16x128_f8f6f4 v[116:119], v[0:7], v[40:47], v[116:119], v238, v238 op_sel_hi:[0,0,0]
	v_mfma_scale_f32_16x16x128_f8f6f4 v[112:115], v[8:15], v[40:47], v[112:115], v238, v238 op_sel_hi:[0,0,0]
	s_waitcnt lgkmcnt(2)
	v_mfma_scale_f32_16x16x128_f8f6f4 v[108:111], v[0:7], v[48:55], v[108:111], v238, v238 op_sel_hi:[0,0,0]
	v_mfma_scale_f32_16x16x128_f8f6f4 v[104:107], v[8:15], v[48:55], v[104:107], v238, v238 op_sel_hi:[0,0,0]
	s_waitcnt lgkmcnt(0)
	v_mfma_scale_f32_16x16x128_f8f6f4 v[100:103], v[0:7], v[56:63], v[100:103], v238, v238 op_sel_hi:[0,0,0]
	v_mfma_scale_f32_16x16x128_f8f6f4 v[96:99], v[8:15], v[56:63], v[96:99], v238, v238 op_sel_hi:[0,0,0]
	s_setprio 0
	s_setprio 1
	v_mfma_scale_f32_16x16x128_f8f6f4 v[92:95], v[16:23], v[32:39], v[92:95], v238, v238 op_sel_hi:[0,0,0]
	v_mfma_scale_f32_16x16x128_f8f6f4 v[88:91], v[24:31], v[32:39], v[88:91], v238, v238 op_sel_hi:[0,0,0]
	v_mfma_scale_f32_16x16x128_f8f6f4 v[84:87], v[16:23], v[40:47], v[84:87], v238, v238 op_sel_hi:[0,0,0]
	v_mfma_scale_f32_16x16x128_f8f6f4 v[80:83], v[24:31], v[40:47], v[80:83], v238, v238 op_sel_hi:[0,0,0]
	v_mfma_scale_f32_16x16x128_f8f6f4 v[76:79], v[16:23], v[48:55], v[76:79], v238, v238 op_sel_hi:[0,0,0]
	v_mfma_scale_f32_16x16x128_f8f6f4 v[72:75], v[24:31], v[48:55], v[72:75], v238, v238 op_sel_hi:[0,0,0]
	v_mfma_scale_f32_16x16x128_f8f6f4 v[68:71], v[16:23], v[56:63], v[68:71], v238, v238 op_sel_hi:[0,0,0]
	v_mfma_scale_f32_16x16x128_f8f6f4 v[64:67], v[24:31], v[56:63], v[64:67], v238, v238 op_sel_hi:[0,0,0]
	s_setprio 0
	s_barrier
	s_add_i32 s82, s82, 2
	s_cmp_ge_u32 s82, s96
	s_cbranch_scc1 .LBB0_1464

.Lc0_moe_1:
	s_setprio 1
	s_waitcnt lgkmcnt(6)
	v_mfma_scale_f32_16x16x128_f8f6f4 v[188:191], v[16:23], v[56:63], 0, v238, v238 op_sel_hi:[0,0,0]
	v_mfma_scale_f32_16x16x128_f8f6f4 v[184:187], v[24:31], v[56:63], 0, v238, v238 op_sel_hi:[0,0,0]
	s_waitcnt lgkmcnt(4)
	v_mfma_scale_f32_16x16x128_f8f6f4 v[180:183], v[16:23], v[48:55], 0, v238, v238 op_sel_hi:[0,0,0]
	v_mfma_scale_f32_16x16x128_f8f6f4 v[176:179], v[24:31], v[48:55], 0, v238, v238 op_sel_hi:[0,0,0]
	s_waitcnt lgkmcnt(2)
	v_mfma_scale_f32_16x16x128_f8f6f4 v[172:175], v[16:23], v[40:47], 0, v238, v238 op_sel_hi:[0,0,0]
	v_mfma_scale_f32_16x16x128_f8f6f4 v[168:171], v[24:31], v[40:47], 0, v238, v238 op_sel_hi:[0,0,0]
	s_waitcnt lgkmcnt(0)
	v_mfma_scale_f32_16x16x128_f8f6f4 v[164:167], v[16:23], v[32:39], 0, v238, v238 op_sel_hi:[0,0,0]
	v_mfma_scale_f32_16x16x128_f8f6f4 v[160:163], v[24:31], v[32:39], 0, v238, v238 op_sel_hi:[0,0,0]
	s_setprio 0
	s_setprio 1
	v_mfma_scale_f32_16x16x128_f8f6f4 v[156:159], v[0:7], v[56:63], 0, v238, v238 op_sel_hi:[0,0,0]
	v_mfma_scale_f32_16x16x128_f8f6f4 v[152:155], v[8:15], v[56:63], 0, v238, v238 op_sel_hi:[0,0,0]
	v_mfma_scale_f32_16x16x128_f8f6f4 v[148:151], v[0:7], v[48:55], 0, v238, v238 op_sel_hi:[0,0,0]
	v_mfma_scale_f32_16x16x128_f8f6f4 v[144:147], v[8:15], v[48:55], 0, v238, v238 op_sel_hi:[0,0,0]
	v_mfma_scale_f32_16x16x128_f8f6f4 v[140:143], v[0:7], v[40:47], 0, v238, v238 op_sel_hi:[0,0,0]
	v_mfma_scale_f32_16x16x128_f8f6f4 v[136:139], v[8:15], v[40:47], 0, v238, v238 op_sel_hi:[0,0,0]
	v_mfma_scale_f32_16x16x128_f8f6f4 v[132:135], v[0:7], v[32:39], 0, v238, v238 op_sel_hi:[0,0,0]
	v_mfma_scale_f32_16x16x128_f8f6f4 v[128:131], v[8:15], v[32:39], 0, v238, v238 op_sel_hi:[0,0,0]
	s_setprio 0
	s_branch .Lc0_moe_1_join
.Lc0_moe_2:
	s_setprio 1
	s_waitcnt lgkmcnt(6)
	v_mfma_scale_f32_16x16x128_f8f6f4 v[124:127], v[16:23], v[32:39], 0, v238, v238 op_sel_hi:[0,0,0]
	v_mfma_scale_f32_16x16x128_f8f6f4 v[120:123], v[24:31], v[32:39], 0, v238, v238 op_sel_hi:[0,0,0]
	s_waitcnt lgkmcnt(4)
	v_mfma_scale_f32_16x16x128_f8f6f4 v[116:119], v[16:23], v[40:47], 0, v238, v238 op_sel_hi:[0,0,0]
	v_mfma_scale_f32_16x16x128_f8f6f4 v[112:115], v[24:31], v[40:47], 0, v238, v238 op_sel_hi:[0,0,0]
	s_waitcnt lgkmcnt(2)
	v_mfma_scale_f32_16x16x128_f8f6f4 v[108:111], v[16:23], v[48:55], 0, v238, v238 op_sel_hi:[0,0,0]
	v_mfma_scale_f32_16x16x128_f8f6f4 v[104:107], v[24:31], v[48:55], 0, v238, v238 op_sel_hi:[0,0,0]
	s_waitcnt lgkmcnt(0)
	v_mfma_scale_f32_16x16x128_f8f6f4 v[100:103], v[16:23], v[56:63], 0, v238, v238 op_sel_hi:[0,0,0]
	v_mfma_scale_f32_16x16x128_f8f6f4 v[96:99], v[24:31], v[56:63], 0, v238, v238 op_sel_hi:[0,0,0]
	s_setprio 0
	s_setprio 1
	v_mfma_scale_f32_16x16x128_f8f6f4 v[92:95], v[0:7], v[32:39], 0, v238, v238 op_sel_hi:[0,0,0]
	v_mfma_scale_f32_16x16x128_f8f6f4 v[88:91], v[8:15], v[32:39], 0, v238, v238 op_sel_hi:[0,0,0]
	v_mfma_scale_f32_16x16x128_f8f6f4 v[84:87], v[0:7], v[40:47], 0, v238, v238 op_sel_hi:[0,0,0]
	v_mfma_scale_f32_16x16x128_f8f6f4 v[80:83], v[8:15], v[40:47], 0, v238, v238 op_sel_hi:[0,0,0]
	v_mfma_scale_f32_16x16x128_f8f6f4 v[76:79], v[0:7], v[48:55], 0, v238, v238 op_sel_hi:[0,0,0]
	v_mfma_scale_f32_16x16x128_f8f6f4 v[72:75], v[8:15], v[48:55], 0, v238, v238 op_sel_hi:[0,0,0]
	v_mfma_scale_f32_16x16x128_f8f6f4 v[68:71], v[0:7], v[56:63], 0, v238, v238 op_sel_hi:[0,0,0]
	v_mfma_scale_f32_16x16x128_f8f6f4 v[64:67], v[8:15], v[56:63], 0, v238, v238 op_sel_hi:[0,0,0]
	s_setprio 0
	s_branch .Lc0_moe_2_join
